# attention unit loop: counted vmcnt(5) instead of vmcnt(0) at the top (do not wait for the previous unit's output stores)
# baseline (speedup 1.0000x reference)
; #define LAS __attribute__((address_space(3)))
; DI void attn_unit(const Args& A, LAS unsigned char* lds, int unit, int tid, int wave, int lane) {
;     const bf16* Z = (const bf16*)(A.ws + WS_Z); bf16* ao = (bf16*)(A.ws + WS_ATTO); float* al = (float*)(A.ws + WS_ATTL);
;     const int x = unit & 15; int r0 = unit >> 4; const int hh = r0 & 3; r0 >>= 2; const int b = r0 % NB, br = r0 / NB;
;     const int dil = br == 0 ? 1 : (br == 1 ? 4 : 16), lsub = SEQ / dil, nblk = lsub / 128;
;     const int res = x / nblk, nbk = x % nblk, l0 = nbk * 128, wbase = l0 - 64;
;     LAS bf16* Qs = (LAS bf16*)(lds + AT_QS); LAS bf16* Ks = (LAS bf16*)(lds + AT_KS); LAS bf16* Vt = (LAS bf16*)(lds + AT_VT); LAS float* btab = (LAS float*)(lds + AT_BT);
;     __syncthreads();
; #pragma unroll
;     for (int i = 0; i < 2; ++i) { const int id = tid + 512 * i, row = id >> 3, ch = id & 7; const int tok = b * SEQ + (l0 + row) * dil + res;
;         *(LAS u32x4_t*)(Qs + row * AT_QLD + ch * 8) = *(const u32x4_t*)(Z + (size_t)tok * ZLD + ZA + hh * 64 + ch * 8); }
;     for (int id = tid; id < 272 * 8; id += NTHR) { const int row = id >> 3, ch = id & 7; const int pos = wbase + row; u32x4_t v = (u32x4_t){0u, 0u, 0u, 0u};
;         if (row < 256 && pos >= 0 && pos < lsub) v = *(const u32x4_t*)(Z + (size_t)(b * SEQ + pos * dil + res) * ZLD + ZA + 256 + hh * 64 + ch * 8);
;         *(LAS u32x4_t*)(Ks + row * AT_QLD + ch * 8) = v; }
;     for (int id = tid; id < 272 * 8; id += NTHR) { const int key = id % 272, ch = id / 272; const int pos = wbase + key; u32x4_t v = (u32x4_t){0u, 0u, 0u, 0u};
;         if (key < 256 && pos >= 0 && pos < lsub) v = *(const u32x4_t*)(Z + (size_t)(b * SEQ + pos * dil + res) * ZLD + ZA + 512 + hh * 64 + ch * 8);
;         LAS bf16* d = Vt + (ch * 8) * AT_VLD + key;
;         d[0] = (bf16)(v.x & 0xffffu); d[AT_VLD] = (bf16)(v.x >> 16); d[2 * AT_VLD] = (bf16)(v.y & 0xffffu); d[3 * AT_VLD] = (bf16)(v.y >> 16);
;         d[4 * AT_VLD] = (bf16)(v.z & 0xffffu); d[5 * AT_VLD] = (bf16)(v.z >> 16); d[6 * AT_VLD] = (bf16)(v.w & 0xffffu); d[7 * AT_VLD] = (bf16)(v.w >> 16); }
;     if (tid < 129) btab[tid] = A.in[I_RELB][t5_bucket((tid - 64) * dil) * 4 + hh] * 1.4426950408889634f;
.LBB0_244:
	s_cmp_lt_i32 s6, 4
	s_cselect_b64 s[0:1], -1, 0
	v_writelane_b32 v235, s0, 60
	s_nop 1
	v_writelane_b32 v235, s1, 61
	s_and_b64 s[0:1], s[0:1], s[2:3]
	s_andn2_b64 vcc, exec, s[0:1]
	v_writelane_b32 v235, s92, 62
	s_cbranch_vccnz .LBB0_496
	s_cmpk_gt_i32 s50, 0xa0
	s_cselect_b32 s0, 0x600, 0
	s_add_i32 s33, s0, s92
	s_cmpk_gt_i32 s33, 0x5ff
	s_mov_b32 s23, 0
	s_cbranch_scc1 .LBB0_336
	s_mov_b32 s6, s33
	s_mov_b32 s7, s50
	s_movk_i32 s8, 0x600
	v_readlane_b32 s9, v235, 52
	v_readlane_b32 s2, v235, 9
	v_readlane_b32 s3, v235, 10
	v_readlane_b32 s4, v235, 19
	v_readlane_b32 s5, v235, 20
	s_mov_b32 s72, 0x3e38aa3b
	s_mov_b32 s73, 0x3e38aa3b
	v_lshrrev_b32_e32 v2, 3, v0
	v_and_b32_e32 v3, 7, v0
	v_lshlrev_b32_e32 v3, 4, v3
	s_movk_i32 s39, 0x90
	v_mad_u32_u24 v1, v2, s39, v3
	v_and_b32_e32 v5, 0xff, v0
	v_lshrrev_b32_e32 v6, 8, v0
	s_movk_i32 s39, 0x1180
	v_mul_u32_u24_e32 v4, s39, v6
	v_lshl_add_u32 v4, v5, 1, v4
	v_add_u32_e32 v4, 0xe100, v4
	v_lshlrev_b32_e32 v6, 4, v6
	v_lshlrev_b32_e32 v8, 2, v5
	v_add_u32_e32 v8, 0x16d00, v8
	v_subrev_u32_e32 v165, 16, v0
	s_movk_i32 s39, 0x81
	v_cmp_gt_u32_e64 s[42:43], s39, v165
	s_movk_i32 s39, 0xa0
	v_cmp_gt_u32_e64 s[48:49], s39, v0
	v_cmp_gt_u32_e64 s[46:47], 64, v0
	v_cmp_gt_u32_e64 s[44:45], 16, v146
	v_subrev_u32_e32 v165, 0x50, v0
	v_cmp_lt_i32_e32 vcc, 0, v165
	v_mov_b32_e32 v7, 0
	s_nop 0
	v_cndmask_b32_e64 v166, 0, 16, vcc
	v_lshlrev_b32_e32 v167, 0, v165
	v_sub_u32_e32 v168, 0, v167
	v_max_i32_e32 v167, v167, v168
	v_cvt_f32_u32_e32 v168, v167
	v_mul_f32_e32 v168, 0x3e000000, v168
	v_max_f32_e32 v168, 1.0, v168
	v_log_f32_e32 v168, v168
	v_cmp_gt_u32_e32 vcc, 8, v167
	v_mul_f32_e32 v168, 0x3f924925, v168
	v_cvt_i32_f32_e32 v168, v168
	v_min_i32_e32 v168, 7, v168
	v_add_u32_e32 v168, 8, v168
	v_cndmask_b32_e32 v168, v168, v167, vcc
	v_add_u32_e32 v168, v168, v166
	v_lshl_or_b32 v7, v168, 0, v7
	v_lshlrev_b32_e32 v167, 2, v165
	v_sub_u32_e32 v168, 0, v167
	v_max_i32_e32 v167, v167, v168
	v_cvt_f32_u32_e32 v168, v167
	v_mul_f32_e32 v168, 0x3e000000, v168
	v_max_f32_e32 v168, 1.0, v168
	v_log_f32_e32 v168, v168
	v_cmp_gt_u32_e32 vcc, 8, v167
	v_mul_f32_e32 v168, 0x3f924925, v168
	v_cvt_i32_f32_e32 v168, v168
	v_min_i32_e32 v168, 7, v168
	v_add_u32_e32 v168, 8, v168
	v_cndmask_b32_e32 v168, v168, v167, vcc
	v_add_u32_e32 v168, v168, v166
	v_lshl_or_b32 v7, v168, 8, v7
	v_lshlrev_b32_e32 v167, 4, v165
	v_sub_u32_e32 v168, 0, v167
	v_max_i32_e32 v167, v167, v168
	v_cvt_f32_u32_e32 v168, v167
	v_mul_f32_e32 v168, 0x3e000000, v168
	v_max_f32_e32 v168, 1.0, v168
	v_log_f32_e32 v168, v168
	v_cmp_gt_u32_e32 vcc, 8, v167
	v_mul_f32_e32 v168, 0x3f924925, v168
	v_cvt_i32_f32_e32 v168, v168
	v_min_i32_e32 v168, 7, v168
	v_add_u32_e32 v168, 8, v168
	v_cndmask_b32_e32 v168, v168, v167, vcc
	v_add_u32_e32 v168, v168, v166
	v_lshl_or_b32 v7, v168, 16, v7
	v_and_b32_e32 v165, 15, v146
	v_lshrrev_b32_e32 v166, 4, v146
	s_lshl_b32 s39, s9, 4
	v_add_u32_e32 v40, s39, v165
	s_movk_i32 s40, 0x90
	v_mul_u32_u24_e32 v34, s40, v40
	v_lshl_add_u32 v34, v166, 4, v34
	v_lshlrev_b32_e32 v167, 2, v166
	v_sub_u32_e32 v35, v167, v165
	v_lshlrev_b32_e32 v35, 2, v35
	v_add_u32_e32 v35, 0x16d40, v35
	v_add_u32_e32 v167, s39, v167
	v_lshlrev_b32_e32 v36, 2, v167
	v_add_u32_e32 v36, 0x16f80, v36
	s_movk_i32 s40, 0x230
	v_mul_u32_u24_e32 v37, s40, v165
	v_lshl_add_u32 v37, v167, 1, v37
	v_add_u32_e32 v37, 0xe100, v37
	v_add_u32_e32 v9, 0x2300, v37
	v_add_u32_e32 v118, 0x4600, v37
	v_add_u32_e32 v144, 0x6900, v37
	v_xor_b32_e32 v38, 16, v146
	v_lshlrev_b32_e32 v38, 2, v38
	v_xor_b32_e32 v39, 32, v146
	v_lshlrev_b32_e32 v39, 2, v39
	v_lshlrev_b32_e32 v41, 3, v166
	v_mov_b32_e32 v232, 0
	v_mov_b32_e32 v233, 0
	s_movk_i32 s40, 0x230
	v_mul_u32_u24_e32 v168, s40, v0
	v_add_u32_e32 v168, 0xe300, v168
	s_and_saveexec_b64 s[40:41], s[46:47]
	ds_write_b64 v168, v[232:233] offset:0
	ds_write_b64 v168, v[232:233] offset:8
	ds_write_b64 v168, v[232:233] offset:16
	ds_write_b64 v168, v[232:233] offset:24
	s_mov_b64 exec, s[40:41]
	s_and_b32 s39, s6, 15
	s_bfe_u32 s40, s6, 0x20004
	s_bfe_u32 s41, s6, 0x30006
	s_lshr_b32 s74, s6, 9
	s_lshl_b32 s75, s74, 1
	s_lshl_b32 s16, 1536, s75
	s_add_i32 s20, s75, 9
	s_add_i32 s26, s75, 4
	s_lshl_b32 s28, s74, 3
	s_lshr_b32 s29, 0x800, s75
	s_add_i32 s17, s29, -1
	s_sub_i32 s76, 4, s75
	s_lshr_b32 s77, s39, s76
	s_lshr_b32 s78, 16, s75
	s_add_i32 s78, s78, -1
	s_and_b32 s78, s39, s78
	s_lshl_b32 s19, s78, 7
	s_add_i32 s18, s19, 0xffffffc0
	s_lshl_b32 s79, s41, 11
	s_add_i32 s79, s79, s77
	s_lshl_b32 s80, s40, 7
	s_lshl_b32 s27, s40, 2
	s_mul_i32 s81, s79, 1536
	s_add_u32 s81, s81, s80
	s_add_u32 s81, s81, 0x28600000
	s_add_u32 s10, s2, s81
	s_addc_u32 s11, s3, 0
	s_lshl_b32 s82, s74, 14
	s_add_i32 s82, s82, s79
	s_lshl_b32 s83, s82, 9
	s_add_u32 s83, s83, s80
	s_add_u32 s83, s83, 0x34a00000
	s_add_u32 s12, s2, s83
	s_addc_u32 s13, s3, 0
	s_lshl_b32 s84, s82, 4
	s_add_u32 s84, s84, s27
	s_add_u32 s84, s84, 0x36200000
	s_add_u32 s14, s2, s84
	s_addc_u32 s15, s3, 0
	v_add_u32_e32 v165, s19, v2
	v_mad_u32_u24 v165, v165, s16, v3
	s_lshl_b32 s85, s16, 6
	global_load_dwordx4 v[120:123], v165, s[10:11]
	v_add_u32_e32 v166, s85, v165
	global_load_dwordx4 v[124:127], v166, s[10:11]
	v_add_u32_e32 v167, s18, v2
	v_med3_i32 v168, v167, 0, s17
	v_mad_u32_u24 v168, v168, s16, v3
	global_load_dwordx4 v[128:131], v168, s[10:11] offset:512
	v_add_u32_e32 v168, 64, v167
	v_med3_i32 v168, v168, 0, s17
	v_mad_u32_u24 v168, v168, s16, v3
	global_load_dwordx4 v[132:135], v168, s[10:11] offset:512
	v_add_u32_e32 v168, 0x80, v167
	v_med3_i32 v168, v168, 0, s17
	v_mad_u32_u24 v168, v168, s16, v3
	global_load_dwordx4 v[136:139], v168, s[10:11] offset:512
	v_add_u32_e32 v168, 0xc0, v167
	v_med3_i32 v168, v168, 0, s17
	v_mad_u32_u24 v168, v168, s16, v3
	global_load_dwordx4 v[140:143], v168, s[10:11] offset:512
	v_add_u32_e32 v169, s18, v5
	v_med3_i32 v169, v169, 0, s17
	v_mad_u32_u24 v169, v169, s16, v6
	global_load_dwordx4 v[148:151], v169, s[10:11] offset:1024
	global_load_dwordx4 v[152:155], v169, s[10:11] offset:1056
	global_load_dwordx4 v[156:159], v169, s[10:11] offset:1088
	global_load_dwordx4 v[160:163], v169, s[10:11] offset:1120
	v_bfe_u32 v171, v7, s28, 8
	v_lshl_add_u32 v171, v171, 4, s27
	s_mov_b64 exec, s[42:43]
	global_load_dword v164, v171, s[4:5]
	s_mov_b64 exec, -1
	s_waitcnt vmcnt(0)
; #define LAS __attribute__((address_space(3)))
; DI void attn_unit(const Args& A, LAS unsigned char* lds, int unit, int tid, int wave, int lane) {
;     ...
;     __syncthreads();
; #pragma unroll
;     for (int i = 0; i < 2; ++i) { const int id = tid + 512 * i, row = id >> 3, ch = id & 7; const int tok = b * SEQ + (l0 + row) * dil + res;
;         *(LAS u32x4_t*)(Qs + row * AT_QLD + ch * 8) = *(const u32x4_t*)(Z + (size_t)tok * ZLD + ZA + hh * 64 + ch * 8); }
;     for (int id = tid; id < 272 * 8; id += NTHR) { const int row = id >> 3, ch = id & 7; const int pos = wbase + row; u32x4_t v = (u32x4_t){0u, 0u, 0u, 0u};
;         if (row < 256 && pos >= 0 && pos < lsub) v = *(const u32x4_t*)(Z + (size_t)(b * SEQ + pos * dil + res) * ZLD + ZA + 256 + hh * 64 + ch * 8);
;         *(LAS u32x4_t*)(Ks + row * AT_QLD + ch * 8) = v; }
;     for (int id = tid; id < 272 * 8; id += NTHR) { const int key = id % 272, ch = id / 272; const int pos = wbase + key; u32x4_t v = (u32x4_t){0u, 0u, 0u, 0u};
;         if (key < 256 && pos >= 0 && pos < lsub) v = *(const u32x4_t*)(Z + (size_t)(b * SEQ + pos * dil + res) * ZLD + ZA + 512 + hh * 64 + ch * 8);
;         LAS bf16* d = Vt + (ch * 8) * AT_VLD + key;
;         d[0] = (bf16)(v.x & 0xffffu); d[AT_VLD] = (bf16)(v.x >> 16); d[2 * AT_VLD] = (bf16)(v.y & 0xffffu); d[3 * AT_VLD] = (bf16)(v.y >> 16);
;         d[4 * AT_VLD] = (bf16)(v.z & 0xffffu); d[5 * AT_VLD] = (bf16)(v.z >> 16); d[6 * AT_VLD] = (bf16)(v.w & 0xffffu); d[7 * AT_VLD] = (bf16)(v.w >> 16); }
;     if (tid < 129) btab[tid] = A.in[I_RELB][t5_bucket((tid - 64) * dil) * 4 + hh] * 1.4426950408889634f;
.LatA_loop:
	s_barrier
	s_mov_b64 s[30:31], s[12:13]
	s_mov_b64 s[32:33], s[14:15]
	s_mov_b32 s34, s19
	s_mov_b32 s35, s20
	s_mov_b32 s36, s26
	s_mov_b32 s37, s18
	s_mov_b32 s38, s29
	v_add_u32_e32 v165, s37, v5
	v_cmp_gt_u32_e32 vcc, s38, v165
	v_mov_b32_e32 v166, 0xf149f2ca
	s_nop 0
	v_cndmask_b32_e64 v165, v166, 0, vcc
	ds_write_b32 v8, v165 offset:640
	s_waitcnt vmcnt(5)
	ds_write_b128 v1, v[120:123]
	ds_write_b128 v1, v[124:127] offset:9216
	ds_write_b128 v1, v[128:131] offset:18432
	ds_write_b128 v1, v[132:135] offset:27648
	ds_write_b128 v1, v[136:139] offset:36864
	ds_write_b128 v1, v[140:143] offset:46080
	ds_write_b16 v4, v148 offset:0
	ds_write_b16_d16_hi v4, v148 offset:560
	ds_write_b16 v4, v149 offset:1120
	ds_write_b16_d16_hi v4, v149 offset:1680
	ds_write_b16 v4, v150 offset:2240
	ds_write_b16_d16_hi v4, v150 offset:2800
	ds_write_b16 v4, v151 offset:3360
	ds_write_b16_d16_hi v4, v151 offset:3920
	ds_write_b16 v4, v152 offset:8960
	ds_write_b16_d16_hi v4, v152 offset:9520
	ds_write_b16 v4, v153 offset:10080
	ds_write_b16_d16_hi v4, v153 offset:10640
	ds_write_b16 v4, v154 offset:11200
	ds_write_b16_d16_hi v4, v154 offset:11760
	ds_write_b16 v4, v155 offset:12320
	ds_write_b16_d16_hi v4, v155 offset:12880
	ds_write_b16 v4, v156 offset:17920
	ds_write_b16_d16_hi v4, v156 offset:18480
	ds_write_b16 v4, v157 offset:19040
	ds_write_b16_d16_hi v4, v157 offset:19600
	ds_write_b16 v4, v158 offset:20160
	ds_write_b16_d16_hi v4, v158 offset:20720
	ds_write_b16 v4, v159 offset:21280
	ds_write_b16_d16_hi v4, v159 offset:21840
	ds_write_b16 v4, v160 offset:26880
	ds_write_b16_d16_hi v4, v160 offset:27440
	ds_write_b16 v4, v161 offset:28000
	ds_write_b16_d16_hi v4, v161 offset:28560
	ds_write_b16 v4, v162 offset:29120
	ds_write_b16_d16_hi v4, v162 offset:29680
	ds_write_b16 v4, v163 offset:30240
	ds_write_b16_d16_hi v4, v163 offset:30800
	v_mul_f32_e32 v167, 0x3fb8aa3b, v164
	v_cndmask_b32_e64 v167, v166, v167, s[42:43]
	s_mov_b64 exec, s[48:49]
	ds_write_b32 v8, v167
	s_mov_b64 exec, -1
	s_add_i32 s6, s6, s7
	s_cmp_lt_i32 s6, s8
	s_cbranch_scc0 .LatA_nopf
	s_and_b32 s39, s6, 15
	s_bfe_u32 s40, s6, 0x20004
	s_bfe_u32 s41, s6, 0x30006
	s_lshr_b32 s74, s6, 9
	s_lshl_b32 s75, s74, 1
	s_lshl_b32 s16, 1536, s75
	s_add_i32 s20, s75, 9
	s_add_i32 s26, s75, 4
	s_lshl_b32 s28, s74, 3
	s_lshr_b32 s29, 0x800, s75
	s_add_i32 s17, s29, -1
	s_sub_i32 s76, 4, s75
	s_lshr_b32 s77, s39, s76
	s_lshr_b32 s78, 16, s75
	s_add_i32 s78, s78, -1
	s_and_b32 s78, s39, s78
	s_lshl_b32 s19, s78, 7
	s_add_i32 s18, s19, 0xffffffc0
	s_lshl_b32 s79, s41, 11
	s_add_i32 s79, s79, s77
	s_lshl_b32 s80, s40, 7
	s_lshl_b32 s27, s40, 2
	s_mul_i32 s81, s79, 1536
	s_add_u32 s81, s81, s80
	s_add_u32 s81, s81, 0x28600000
	s_add_u32 s10, s2, s81
	s_addc_u32 s11, s3, 0
	s_lshl_b32 s82, s74, 14
	s_add_i32 s82, s82, s79
	s_lshl_b32 s83, s82, 9
	s_add_u32 s83, s83, s80
	s_add_u32 s83, s83, 0x34a00000
	s_add_u32 s12, s2, s83
	s_addc_u32 s13, s3, 0
	s_lshl_b32 s84, s82, 4
	s_add_u32 s84, s84, s27
	s_add_u32 s84, s84, 0x36200000
	s_add_u32 s14, s2, s84
	s_addc_u32 s15, s3, 0
	v_add_u32_e32 v165, s19, v2
	v_mad_u32_u24 v165, v165, s16, v3
	s_lshl_b32 s85, s16, 6
	global_load_dwordx4 v[120:123], v165, s[10:11]
	v_add_u32_e32 v166, s85, v165
	global_load_dwordx4 v[124:127], v166, s[10:11]
	v_add_u32_e32 v167, s18, v2
	v_med3_i32 v168, v167, 0, s17
	v_mad_u32_u24 v168, v168, s16, v3
	global_load_dwordx4 v[128:131], v168, s[10:11] offset:512
	v_add_u32_e32 v168, 64, v167
	v_med3_i32 v168, v168, 0, s17
	v_mad_u32_u24 v168, v168, s16, v3
	global_load_dwordx4 v[132:135], v168, s[10:11] offset:512
	v_add_u32_e32 v168, 0x80, v167
	v_med3_i32 v168, v168, 0, s17
	v_mad_u32_u24 v168, v168, s16, v3
	global_load_dwordx4 v[136:139], v168, s[10:11] offset:512
	v_add_u32_e32 v168, 0xc0, v167
	v_med3_i32 v168, v168, 0, s17
	v_mad_u32_u24 v168, v168, s16, v3
	global_load_dwordx4 v[140:143], v168, s[10:11] offset:512
	v_add_u32_e32 v169, s18, v5
	v_med3_i32 v169, v169, 0, s17
	v_mad_u32_u24 v169, v169, s16, v6
	global_load_dwordx4 v[148:151], v169, s[10:11] offset:1024
	global_load_dwordx4 v[152:155], v169, s[10:11] offset:1056
	global_load_dwordx4 v[156:159], v169, s[10:11] offset:1088
	global_load_dwordx4 v[160:163], v169, s[10:11] offset:1120
	v_bfe_u32 v171, v7, s28, 8
	v_lshl_add_u32 v171, v171, 4, s27
	s_mov_b64 exec, s[42:43]
	global_load_dword v164, v171, s[4:5]
	s_mov_b64 exec, -1

; #define LAS __attribute__((address_space(3)))
; DI void attn_unit(const Args& A, LAS unsigned char* lds, int unit, int tid, int wave, int lane) {
;     const bf16* Z = (const bf16*)(A.ws + WS_Z); bf16* ao = (bf16*)(A.ws + WS_ATTO); float* al = (float*)(A.ws + WS_ATTL);
;     const int x = unit & 15; int r0 = unit >> 4; const int hh = r0 & 3; r0 >>= 2; const int b = r0 % NB, br = r0 / NB;
;     const int dil = br == 0 ? 1 : (br == 1 ? 4 : 16), lsub = SEQ / dil, nblk = lsub / 128;
;     const int res = x / nblk, nbk = x % nblk, l0 = nbk * 128, wbase = l0 - 64;
;     LAS bf16* Qs = (LAS bf16*)(lds + AT_QS); LAS bf16* Ks = (LAS bf16*)(lds + AT_KS); LAS bf16* Vt = (LAS bf16*)(lds + AT_VT); LAS float* btab = (LAS float*)(lds + AT_BT);
;     __syncthreads();
; #pragma unroll
;     for (int i = 0; i < 2; ++i) { const int id = tid + 512 * i, row = id >> 3, ch = id & 7; const int tok = b * SEQ + (l0 + row) * dil + res;
;         *(LAS u32x4_t*)(Qs + row * AT_QLD + ch * 8) = *(const u32x4_t*)(Z + (size_t)tok * ZLD + ZA + hh * 64 + ch * 8); }
;     for (int id = tid; id < 272 * 8; id += NTHR) { const int row = id >> 3, ch = id & 7; const int pos = wbase + row; u32x4_t v = (u32x4_t){0u, 0u, 0u, 0u};
;         if (row < 256 && pos >= 0 && pos < lsub) v = *(const u32x4_t*)(Z + (size_t)(b * SEQ + pos * dil + res) * ZLD + ZA + 256 + hh * 64 + ch * 8);
;         *(LAS u32x4_t*)(Ks + row * AT_QLD + ch * 8) = v; }
;     for (int id = tid; id < 272 * 8; id += NTHR) { const int key = id % 272, ch = id / 272; const int pos = wbase + key; u32x4_t v = (u32x4_t){0u, 0u, 0u, 0u};
;         if (key < 256 && pos >= 0 && pos < lsub) v = *(const u32x4_t*)(Z + (size_t)(b * SEQ + pos * dil + res) * ZLD + ZA + 512 + hh * 64 + ch * 8);
;         LAS bf16* d = Vt + (ch * 8) * AT_VLD + key;
;         d[0] = (bf16)(v.x & 0xffffu); d[AT_VLD] = (bf16)(v.x >> 16); d[2 * AT_VLD] = (bf16)(v.y & 0xffffu); d[3 * AT_VLD] = (bf16)(v.y >> 16);
;         d[4 * AT_VLD] = (bf16)(v.z & 0xffffu); d[5 * AT_VLD] = (bf16)(v.z >> 16); d[6 * AT_VLD] = (bf16)(v.w & 0xffffu); d[7 * AT_VLD] = (bf16)(v.w >> 16); }
;     if (tid < 129) btab[tid] = A.in[I_RELB][t5_bucket((tid - 64) * dil) * 4 + hh] * 1.4426950408889634f;
.Latmap_s22:
	v_readlane_b32 s9, v235, 52
	v_readlane_b32 s2, v235, 9
	v_readlane_b32 s3, v235, 10
	v_readlane_b32 s4, v235, 19
	v_readlane_b32 s5, v235, 20
	s_mov_b32 s72, 0x3e38aa3b
	s_mov_b32 s73, 0x3e38aa3b
	v_lshrrev_b32_e32 v2, 3, v0
	v_and_b32_e32 v3, 7, v0
	v_lshlrev_b32_e32 v3, 4, v3
	s_movk_i32 s39, 0x90
	v_mad_u32_u24 v1, v2, s39, v3
	v_and_b32_e32 v5, 0xff, v0
	v_lshrrev_b32_e32 v6, 8, v0
	s_movk_i32 s39, 0x1180
	v_mul_u32_u24_e32 v4, s39, v6
	v_lshl_add_u32 v4, v5, 1, v4
	v_add_u32_e32 v4, 0xe100, v4
	v_lshlrev_b32_e32 v6, 4, v6
	v_lshlrev_b32_e32 v8, 2, v5
	v_add_u32_e32 v8, 0x16d00, v8
	v_subrev_u32_e32 v165, 16, v0
	s_movk_i32 s39, 0x81
	v_cmp_gt_u32_e64 s[42:43], s39, v165
	s_movk_i32 s39, 0xa0
	v_cmp_gt_u32_e64 s[48:49], s39, v0
	v_cmp_gt_u32_e64 s[46:47], 64, v0
	v_cmp_gt_u32_e64 s[44:45], 16, v146
	v_subrev_u32_e32 v165, 0x50, v0
	v_cmp_lt_i32_e32 vcc, 0, v165
	v_mov_b32_e32 v7, 0
	s_nop 0
	v_cndmask_b32_e64 v166, 0, 16, vcc
	v_lshlrev_b32_e32 v167, 0, v165
	v_sub_u32_e32 v168, 0, v167
	v_max_i32_e32 v167, v167, v168
	v_cvt_f32_u32_e32 v168, v167
	v_mul_f32_e32 v168, 0x3e000000, v168
	v_max_f32_e32 v168, 1.0, v168
	v_log_f32_e32 v168, v168
	v_cmp_gt_u32_e32 vcc, 8, v167
	v_mul_f32_e32 v168, 0x3f924925, v168
	v_cvt_i32_f32_e32 v168, v168
	v_min_i32_e32 v168, 7, v168
	v_add_u32_e32 v168, 8, v168
	v_cndmask_b32_e32 v168, v168, v167, vcc
	v_add_u32_e32 v168, v168, v166
	v_lshl_or_b32 v7, v168, 0, v7
	v_lshlrev_b32_e32 v167, 2, v165
	v_sub_u32_e32 v168, 0, v167
	v_max_i32_e32 v167, v167, v168
	v_cvt_f32_u32_e32 v168, v167
	v_mul_f32_e32 v168, 0x3e000000, v168
	v_max_f32_e32 v168, 1.0, v168
	v_log_f32_e32 v168, v168
	v_cmp_gt_u32_e32 vcc, 8, v167
	v_mul_f32_e32 v168, 0x3f924925, v168
	v_cvt_i32_f32_e32 v168, v168
	v_min_i32_e32 v168, 7, v168
	v_add_u32_e32 v168, 8, v168
	v_cndmask_b32_e32 v168, v168, v167, vcc
	v_add_u32_e32 v168, v168, v166
	v_lshl_or_b32 v7, v168, 8, v7
	v_lshlrev_b32_e32 v167, 4, v165
	v_sub_u32_e32 v168, 0, v167
	v_max_i32_e32 v167, v167, v168
	v_cvt_f32_u32_e32 v168, v167
	v_mul_f32_e32 v168, 0x3e000000, v168
	v_max_f32_e32 v168, 1.0, v168
	v_log_f32_e32 v168, v168
	v_cmp_gt_u32_e32 vcc, 8, v167
	v_mul_f32_e32 v168, 0x3f924925, v168
	v_cvt_i32_f32_e32 v168, v168
	v_min_i32_e32 v168, 7, v168
	v_add_u32_e32 v168, 8, v168
	v_cndmask_b32_e32 v168, v168, v167, vcc
	v_add_u32_e32 v168, v168, v166
	v_lshl_or_b32 v7, v168, 16, v7
	v_and_b32_e32 v165, 15, v146
	v_lshrrev_b32_e32 v166, 4, v146
	s_lshl_b32 s39, s9, 4
	v_add_u32_e32 v40, s39, v165
	s_movk_i32 s40, 0x90
	v_mul_u32_u24_e32 v34, s40, v40
	v_lshl_add_u32 v34, v166, 4, v34
	v_lshlrev_b32_e32 v167, 2, v166
	v_sub_u32_e32 v35, v167, v165
	v_lshlrev_b32_e32 v35, 2, v35
	v_add_u32_e32 v35, 0x16d40, v35
	v_add_u32_e32 v167, s39, v167
	v_lshlrev_b32_e32 v36, 2, v167
	v_add_u32_e32 v36, 0x16f80, v36
	s_movk_i32 s40, 0x230
	v_mul_u32_u24_e32 v37, s40, v165
	v_lshl_add_u32 v37, v167, 1, v37
	v_add_u32_e32 v37, 0xe100, v37
	v_add_u32_e32 v9, 0x2300, v37
	v_add_u32_e32 v118, 0x4600, v37
	v_add_u32_e32 v144, 0x6900, v37
	v_xor_b32_e32 v38, 16, v146
	v_lshlrev_b32_e32 v38, 2, v38
	v_xor_b32_e32 v39, 32, v146
	v_lshlrev_b32_e32 v39, 2, v39
	v_lshlrev_b32_e32 v41, 3, v166
	v_mov_b32_e32 v232, 0
	v_mov_b32_e32 v233, 0
	s_movk_i32 s40, 0x230
	v_mul_u32_u24_e32 v168, s40, v0
	v_add_u32_e32 v168, 0xe300, v168
	s_and_saveexec_b64 s[40:41], s[46:47]
	ds_write_b64 v168, v[232:233] offset:0
	ds_write_b64 v168, v[232:233] offset:8
	ds_write_b64 v168, v[232:233] offset:16
	ds_write_b64 v168, v[232:233] offset:24
	s_mov_b64 exec, s[40:41]
	s_and_b32 s39, s6, 15
	s_bfe_u32 s40, s6, 0x20004
	s_bfe_u32 s41, s6, 0x30006
	s_lshr_b32 s74, s6, 9
	s_lshl_b32 s75, s74, 1
	s_lshl_b32 s16, 1536, s75
	s_add_i32 s20, s75, 9
	s_add_i32 s26, s75, 4
	s_lshl_b32 s28, s74, 3
	s_lshr_b32 s29, 0x800, s75
	s_add_i32 s17, s29, -1
	s_sub_i32 s76, 4, s75
	s_lshr_b32 s77, s39, s76
	s_lshr_b32 s78, 16, s75
	s_add_i32 s78, s78, -1
	s_and_b32 s78, s39, s78
	s_lshl_b32 s19, s78, 7
	s_add_i32 s18, s19, 0xffffffc0
	s_lshl_b32 s79, s41, 11
	s_add_i32 s79, s79, s77
	s_lshl_b32 s80, s40, 7
	s_lshl_b32 s27, s40, 2
	s_mul_i32 s81, s79, 1536
	s_add_u32 s81, s81, s80
	s_add_u32 s81, s81, 0x28600000
	s_add_u32 s10, s2, s81
	s_addc_u32 s11, s3, 0
	s_lshl_b32 s82, s74, 14
	s_add_i32 s82, s82, s79
	s_lshl_b32 s83, s82, 9
	s_add_u32 s83, s83, s80
	s_add_u32 s83, s83, 0x34a00000
	s_add_u32 s12, s2, s83
	s_addc_u32 s13, s3, 0
	s_lshl_b32 s84, s82, 4
	s_add_u32 s84, s84, s27
	s_add_u32 s84, s84, 0x36200000
	s_add_u32 s14, s2, s84
	s_addc_u32 s15, s3, 0
	v_add_u32_e32 v165, s19, v2
	v_mad_u32_u24 v165, v165, s16, v3
	s_lshl_b32 s85, s16, 6
	global_load_dwordx4 v[120:123], v165, s[10:11]
	v_add_u32_e32 v166, s85, v165
	global_load_dwordx4 v[124:127], v166, s[10:11]
	v_add_u32_e32 v167, s18, v2
	v_med3_i32 v168, v167, 0, s17
	v_mad_u32_u24 v168, v168, s16, v3
	global_load_dwordx4 v[128:131], v168, s[10:11] offset:512
	v_add_u32_e32 v168, 64, v167
	v_med3_i32 v168, v168, 0, s17
	v_mad_u32_u24 v168, v168, s16, v3
	global_load_dwordx4 v[132:135], v168, s[10:11] offset:512
	v_add_u32_e32 v168, 0x80, v167
	v_med3_i32 v168, v168, 0, s17
	v_mad_u32_u24 v168, v168, s16, v3
	global_load_dwordx4 v[136:139], v168, s[10:11] offset:512
	v_add_u32_e32 v168, 0xc0, v167
	v_med3_i32 v168, v168, 0, s17
	v_mad_u32_u24 v168, v168, s16, v3
	global_load_dwordx4 v[140:143], v168, s[10:11] offset:512
	v_add_u32_e32 v169, s18, v5
	v_med3_i32 v169, v169, 0, s17
	v_mad_u32_u24 v169, v169, s16, v6
	global_load_dwordx4 v[148:151], v169, s[10:11] offset:1024
	global_load_dwordx4 v[152:155], v169, s[10:11] offset:1056
	global_load_dwordx4 v[156:159], v169, s[10:11] offset:1088
	global_load_dwordx4 v[160:163], v169, s[10:11] offset:1120
	v_bfe_u32 v171, v7, s28, 8
	v_lshl_add_u32 v171, v171, 4, s27
	s_mov_b64 exec, s[42:43]
	global_load_dword v164, v171, s[4:5]
	s_mov_b64 exec, -1
	s_waitcnt vmcnt(0)

; #define LAS __attribute__((address_space(3)))
; DI void attn_unit(const Args& A, LAS unsigned char* lds, int unit, int tid, int wave, int lane) {
;     const bf16* Z = (const bf16*)(A.ws + WS_Z); bf16* ao = (bf16*)(A.ws + WS_ATTO); float* al = (float*)(A.ws + WS_ATTL);
;     const int x = unit & 15; int r0 = unit >> 4; const int hh = r0 & 3; r0 >>= 2; const int b = r0 % NB, br = r0 / NB;
;     const int dil = br == 0 ? 1 : (br == 1 ? 4 : 16), lsub = SEQ / dil, nblk = lsub / 128;
;     const int res = x / nblk, nbk = x % nblk, l0 = nbk * 128, wbase = l0 - 64;
;     LAS bf16* Qs = (LAS bf16*)(lds + AT_QS); LAS bf16* Ks = (LAS bf16*)(lds + AT_KS); LAS bf16* Vt = (LAS bf16*)(lds + AT_VT); LAS float* btab = (LAS float*)(lds + AT_BT);
;     __syncthreads();
; #pragma unroll
;     for (int i = 0; i < 2; ++i) { const int id = tid + 512 * i, row = id >> 3, ch = id & 7; const int tok = b * SEQ + (l0 + row) * dil + res;
;         *(LAS u32x4_t*)(Qs + row * AT_QLD + ch * 8) = *(const u32x4_t*)(Z + (size_t)tok * ZLD + ZA + hh * 64 + ch * 8); }
;     for (int id = tid; id < 272 * 8; id += NTHR) { const int row = id >> 3, ch = id & 7; const int pos = wbase + row; u32x4_t v = (u32x4_t){0u, 0u, 0u, 0u};
;         if (row < 256 && pos >= 0 && pos < lsub) v = *(const u32x4_t*)(Z + (size_t)(b * SEQ + pos * dil + res) * ZLD + ZA + 256 + hh * 64 + ch * 8);
;         *(LAS u32x4_t*)(Ks + row * AT_QLD + ch * 8) = v; }
;     for (int id = tid; id < 272 * 8; id += NTHR) { const int key = id % 272, ch = id / 272; const int pos = wbase + key; u32x4_t v = (u32x4_t){0u, 0u, 0u, 0u};
;         if (key < 256 && pos >= 0 && pos < lsub) v = *(const u32x4_t*)(Z + (size_t)(b * SEQ + pos * dil + res) * ZLD + ZA + 512 + hh * 64 + ch * 8);
;         LAS bf16* d = Vt + (ch * 8) * AT_VLD + key;
;         d[0] = (bf16)(v.x & 0xffffu); d[AT_VLD] = (bf16)(v.x >> 16); d[2 * AT_VLD] = (bf16)(v.y & 0xffffu); d[3 * AT_VLD] = (bf16)(v.y >> 16);
;         d[4 * AT_VLD] = (bf16)(v.z & 0xffffu); d[5 * AT_VLD] = (bf16)(v.z >> 16); d[6 * AT_VLD] = (bf16)(v.w & 0xffffu); d[7 * AT_VLD] = (bf16)(v.w >> 16); }
;     if (tid < 129) btab[tid] = A.in[I_RELB][t5_bucket((tid - 64) * dil) * 4 + hh] * 1.4426950408889634f;
.LBB0_1704:
	s_cmp_lt_i32 s6, 14
	s_cselect_b64 s[0:1], -1, 0
	v_writelane_b32 v234, s0, 44
	s_nop 1
	v_writelane_b32 v234, s1, 45
	s_and_b64 s[0:1], s[0:1], s[2:3]
	s_andn2_b64 vcc, exec, s[0:1]
	s_cbranch_vccnz .LBB0_1958
	s_cmpk_gt_i32 s50, 0xa0
	s_cselect_b32 s0, 0x600, 0
	s_add_i32 s33, s0, s92
	s_cmpk_gt_i32 s33, 0x5ff
	s_mov_b32 s3, 0
	s_cbranch_scc1 .LBB0_1796
	s_mov_b32 s6, s33
	s_mov_b32 s7, s50
	s_movk_i32 s8, 0x600
	v_readlane_b32 s9, v235, 52
	v_readlane_b32 s2, v235, 9
	v_readlane_b32 s3, v235, 10
	v_readlane_b32 s4, v235, 19
	v_readlane_b32 s5, v235, 20
	s_mov_b32 s72, 0x3e38aa3b
	s_mov_b32 s73, 0x3e38aa3b
	v_lshrrev_b32_e32 v2, 3, v0
	v_and_b32_e32 v3, 7, v0
	v_lshlrev_b32_e32 v3, 4, v3
	s_movk_i32 s39, 0x90
	v_mad_u32_u24 v1, v2, s39, v3
	v_and_b32_e32 v5, 0xff, v0
	v_lshrrev_b32_e32 v6, 8, v0
	s_movk_i32 s39, 0x1180
	v_mul_u32_u24_e32 v4, s39, v6
	v_lshl_add_u32 v4, v5, 1, v4
	v_add_u32_e32 v4, 0xe100, v4
	v_lshlrev_b32_e32 v6, 4, v6
	v_lshlrev_b32_e32 v8, 2, v5
	v_add_u32_e32 v8, 0x16d00, v8
	v_subrev_u32_e32 v165, 16, v0
	s_movk_i32 s39, 0x81
	v_cmp_gt_u32_e64 s[42:43], s39, v165
	s_movk_i32 s39, 0xa0
	v_cmp_gt_u32_e64 s[48:49], s39, v0
	v_cmp_gt_u32_e64 s[46:47], 64, v0
	v_cmp_gt_u32_e64 s[44:45], 16, v146
	v_subrev_u32_e32 v165, 0x50, v0
	v_cmp_lt_i32_e32 vcc, 0, v165
	v_mov_b32_e32 v7, 0
	s_nop 0
	v_cndmask_b32_e64 v166, 0, 16, vcc
	v_lshlrev_b32_e32 v167, 0, v165
	v_sub_u32_e32 v168, 0, v167
	v_max_i32_e32 v167, v167, v168
	v_cvt_f32_u32_e32 v168, v167
	v_mul_f32_e32 v168, 0x3e000000, v168
	v_max_f32_e32 v168, 1.0, v168
	v_log_f32_e32 v168, v168
	v_cmp_gt_u32_e32 vcc, 8, v167
	v_mul_f32_e32 v168, 0x3f924925, v168
	v_cvt_i32_f32_e32 v168, v168
	v_min_i32_e32 v168, 7, v168
	v_add_u32_e32 v168, 8, v168
	v_cndmask_b32_e32 v168, v168, v167, vcc
	v_add_u32_e32 v168, v168, v166
	v_lshl_or_b32 v7, v168, 0, v7
	v_lshlrev_b32_e32 v167, 2, v165
	v_sub_u32_e32 v168, 0, v167
	v_max_i32_e32 v167, v167, v168
	v_cvt_f32_u32_e32 v168, v167
	v_mul_f32_e32 v168, 0x3e000000, v168
	v_max_f32_e32 v168, 1.0, v168
	v_log_f32_e32 v168, v168
	v_cmp_gt_u32_e32 vcc, 8, v167
	v_mul_f32_e32 v168, 0x3f924925, v168
	v_cvt_i32_f32_e32 v168, v168
	v_min_i32_e32 v168, 7, v168
	v_add_u32_e32 v168, 8, v168
	v_cndmask_b32_e32 v168, v168, v167, vcc
	v_add_u32_e32 v168, v168, v166
	v_lshl_or_b32 v7, v168, 8, v7
	v_lshlrev_b32_e32 v167, 4, v165
	v_sub_u32_e32 v168, 0, v167
	v_max_i32_e32 v167, v167, v168
	v_cvt_f32_u32_e32 v168, v167
	v_mul_f32_e32 v168, 0x3e000000, v168
	v_max_f32_e32 v168, 1.0, v168
	v_log_f32_e32 v168, v168
	v_cmp_gt_u32_e32 vcc, 8, v167
	v_mul_f32_e32 v168, 0x3f924925, v168
	v_cvt_i32_f32_e32 v168, v168
	v_min_i32_e32 v168, 7, v168
	v_add_u32_e32 v168, 8, v168
	v_cndmask_b32_e32 v168, v168, v167, vcc
	v_add_u32_e32 v168, v168, v166
	v_lshl_or_b32 v7, v168, 16, v7
	v_and_b32_e32 v165, 15, v146
	v_lshrrev_b32_e32 v166, 4, v146
	s_lshl_b32 s39, s9, 4
	v_add_u32_e32 v40, s39, v165
	s_movk_i32 s40, 0x90
	v_mul_u32_u24_e32 v34, s40, v40
	v_lshl_add_u32 v34, v166, 4, v34
	v_lshlrev_b32_e32 v167, 2, v166
	v_sub_u32_e32 v35, v167, v165
	v_lshlrev_b32_e32 v35, 2, v35
	v_add_u32_e32 v35, 0x16d40, v35
	v_add_u32_e32 v167, s39, v167
	v_lshlrev_b32_e32 v36, 2, v167
	v_add_u32_e32 v36, 0x16f80, v36
	s_movk_i32 s40, 0x230
	v_mul_u32_u24_e32 v37, s40, v165
	v_lshl_add_u32 v37, v167, 1, v37
	v_add_u32_e32 v37, 0xe100, v37
	v_add_u32_e32 v9, 0x2300, v37
	v_add_u32_e32 v118, 0x4600, v37
	v_add_u32_e32 v144, 0x6900, v37
	v_xor_b32_e32 v38, 16, v146
	v_lshlrev_b32_e32 v38, 2, v38
	v_xor_b32_e32 v39, 32, v146
	v_lshlrev_b32_e32 v39, 2, v39
	v_lshlrev_b32_e32 v41, 3, v166
	v_mov_b32_e32 v232, 0
	v_mov_b32_e32 v233, 0
	s_movk_i32 s40, 0x230
	v_mul_u32_u24_e32 v168, s40, v0
	v_add_u32_e32 v168, 0xe300, v168
	s_and_saveexec_b64 s[40:41], s[46:47]
	ds_write_b64 v168, v[232:233] offset:0
	ds_write_b64 v168, v[232:233] offset:8
	ds_write_b64 v168, v[232:233] offset:16
	ds_write_b64 v168, v[232:233] offset:24
	s_mov_b64 exec, s[40:41]
	s_and_b32 s39, s6, 15
	s_bfe_u32 s40, s6, 0x20004
	s_bfe_u32 s41, s6, 0x30006
	s_lshr_b32 s74, s6, 9
	s_lshl_b32 s75, s74, 1
	s_lshl_b32 s16, 1536, s75
	s_add_i32 s20, s75, 9
	s_add_i32 s26, s75, 4
	s_lshl_b32 s28, s74, 3
	s_lshr_b32 s29, 0x800, s75
	s_add_i32 s17, s29, -1
	s_sub_i32 s76, 4, s75
	s_lshr_b32 s77, s39, s76
	s_lshr_b32 s78, 16, s75
	s_add_i32 s78, s78, -1
	s_and_b32 s78, s39, s78
	s_lshl_b32 s19, s78, 7
	s_add_i32 s18, s19, 0xffffffc0
	s_lshl_b32 s79, s41, 11
	s_add_i32 s79, s79, s77
	s_lshl_b32 s80, s40, 7
	s_lshl_b32 s27, s40, 2
	s_mul_i32 s81, s79, 1536
	s_add_u32 s81, s81, s80
	s_add_u32 s81, s81, 0x28600000
	s_add_u32 s10, s2, s81
	s_addc_u32 s11, s3, 0
	s_lshl_b32 s82, s74, 14
	s_add_i32 s82, s82, s79
	s_lshl_b32 s83, s82, 9
	s_add_u32 s83, s83, s80
	s_add_u32 s83, s83, 0x34a00000
	s_add_u32 s12, s2, s83
	s_addc_u32 s13, s3, 0
	s_lshl_b32 s84, s82, 4
	s_add_u32 s84, s84, s27
	s_add_u32 s84, s84, 0x36200000
	s_add_u32 s14, s2, s84
	s_addc_u32 s15, s3, 0
	v_add_u32_e32 v165, s19, v2
	v_mad_u32_u24 v165, v165, s16, v3
	s_lshl_b32 s85, s16, 6
	global_load_dwordx4 v[120:123], v165, s[10:11]
	v_add_u32_e32 v166, s85, v165
	global_load_dwordx4 v[124:127], v166, s[10:11]
	v_add_u32_e32 v167, s18, v2
	v_med3_i32 v168, v167, 0, s17
	v_mad_u32_u24 v168, v168, s16, v3
	global_load_dwordx4 v[128:131], v168, s[10:11] offset:512
	v_add_u32_e32 v168, 64, v167
	v_med3_i32 v168, v168, 0, s17
	v_mad_u32_u24 v168, v168, s16, v3
	global_load_dwordx4 v[132:135], v168, s[10:11] offset:512
	v_add_u32_e32 v168, 0x80, v167
	v_med3_i32 v168, v168, 0, s17
	v_mad_u32_u24 v168, v168, s16, v3
	global_load_dwordx4 v[136:139], v168, s[10:11] offset:512
	v_add_u32_e32 v168, 0xc0, v167
	v_med3_i32 v168, v168, 0, s17
	v_mad_u32_u24 v168, v168, s16, v3
	global_load_dwordx4 v[140:143], v168, s[10:11] offset:512
	v_add_u32_e32 v169, s18, v5
	v_med3_i32 v169, v169, 0, s17
	v_mad_u32_u24 v169, v169, s16, v6
	global_load_dwordx4 v[148:151], v169, s[10:11] offset:1024
	global_load_dwordx4 v[152:155], v169, s[10:11] offset:1056
	global_load_dwordx4 v[156:159], v169, s[10:11] offset:1088
	global_load_dwordx4 v[160:163], v169, s[10:11] offset:1120
	v_bfe_u32 v171, v7, s28, 8
	v_lshl_add_u32 v171, v171, 4, s27
	s_mov_b64 exec, s[42:43]
	global_load_dword v164, v171, s[4:5]
	s_mov_b64 exec, -1
	s_waitcnt vmcnt(0)
